# top-k: odd workgroups run their context unit before the latent unit so the two halves' bandwidth-bound gathers are staggered
# speedup vs baseline: 1.0063x; 1.0063x over previous
.LBB0_1317:
	s_or_b64 exec, exec, s[4:5]
	v_readlane_b32 s6, v254, 26
	v_readlane_b32 s7, v254, 27
	s_and_b64 s[6:7], s[6:7], exec
	s_movk_i32 s1, 0x200
	s_mov_b64 s[4:5], s[96:97]
	s_waitcnt vmcnt(12)
	v_mov_b32_e32 v78, v0
	s_cselect_b32 s1, 0x100, s1
	s_mov_b32 s2, s80
	s_movk_i32 s100, 0x100
	s_bitcmp1_b32 s80, 0
	s_cbranch_scc0 .Lmy_tkf
	s_cmp_gt_u32 s1, 0x100
	s_cbranch_scc0 .Lmy_tkf
	s_add_i32 s2, s80, 0x100
	s_mov_b32 s100, 0xffffff00
.Lmy_tkf:
	s_waitcnt lgkmcnt(0)
	s_barrier
	s_cmp_ge_i32 s2, s1
	s_cbranch_scc1 .LBB0_1360
	s_load_dwordx2 s[6:7], s[4:5], 0xe0
	s_waitcnt vmcnt(0)
	v_and_b32_e32 v80, 63, v78
	v_lshlrev_b32_e32 v62, 4, v80
	v_mov_b32_e32 v63, v131
	v_ashrrev_i32_e32 v79, 6, v78
	s_waitcnt lgkmcnt(0)
	s_add_u32 s22, s6, 0x70d68000
	s_addc_u32 s27, s7, 0
	s_add_u32 s29, s6, 0x70fa8000
	v_lshl_add_u64 v[4:5], s[6:7], 0, v[62:63]
	s_mov_b64 s[4:5], 0x41068000
	v_lshlrev_b32_e32 v2, 4, v79
	s_addc_u32 s33, s7, 0
	v_lshl_add_u64 v[64:65], v[4:5], 0, s[4:5]
	v_lshlrev_b32_e32 v4, 2, v79
	s_add_u32 s14, s6, 0x711e8000
	v_or_b32_e32 v6, 1, v4
	v_ashrrev_i32_e32 v3, 31, v2
	s_addc_u32 s15, s7, 0
	v_ashrrev_i32_e32 v5, 31, v4
	v_ashrrev_i32_e32 v7, 31, v6
	v_add_u32_e32 v84, 0xffffff80, v2
	v_lshlrev_b64 v[2:3], 10, v[2:3]
	s_add_u32 s16, s6, 0x63568000
	v_lshlrev_b64 v[66:67], 10, v[4:5]
	v_lshlrev_b64 v[68:69], 10, v[6:7]
	v_or_b32_e32 v6, 2, v4
	v_or_b32_e32 v4, 3, v4
	v_or_b32_e32 v2, v2, v62
	s_addc_u32 s17, s7, 0
	v_ashrrev_i32_e32 v7, 31, v6
	v_ashrrev_i32_e32 v5, 31, v4
	v_lshl_add_u64 v[2:3], s[6:7], 0, v[2:3]
	s_mov_b64 s[6:7], 0x6356bc00
	v_lshl_add_u32 v81, v79, 5, 0
	v_cmp_gt_i32_e64 s[4:5], 16, v79
	v_lshlrev_b64 v[70:71], 10, v[6:7]
	v_lshlrev_b64 v[72:73], 10, v[4:5]
	v_lshl_add_u32 v82, v78, 3, 0
	v_not_b32_e32 v83, v78
	v_lshl_add_u64 v[74:75], v[2:3], 0, s[6:7]
	v_lshl_add_u32 v85, v79, 7, 0
	s_branch .LBB0_1320
.LBB0_1319:
	s_mov_b32 s6, s100
	s_add_i32 s2, s6, s2
	s_cmp_lt_u32 s2, s1
	s_cbranch_scc0 .LBB0_1360
